# speedup vs baseline: 1.0168x; 1.0168x over previous
.Lpc_anchor:
	s_add_u32 s44, s44, _Z7dog_finPKfS0_Pf-.Lpc_anchor
	s_addc_u32 s45, s45, 0
	s_load_dwordx16 s[48:63], s[44:45], 0x0
	s_load_dwordx16 s[64:79], s[44:45], 0x40
	s_load_dwordx16 s[80:95], s[44:45], 0x80
	v_mul_f32_e32 v16, v12, v12
	v_add_f32_e32 v17, 0x3f800000, v12
	v_add_f32_e32 v18, 0x40000000, v12
	v_add_f32_e32 v19, 0x40400000, v12
	v_mul_f32_e32 v17, v17, v17
	v_mul_f32_e32 v18, v18, v18
	v_mul_f32_e32 v19, v19, v19
	v_mul_f32_e32 v20, v8, v16
	v_mul_f32_e32 v24, v9, v16
	v_mul_f32_e32 v21, v8, v17
	v_mul_f32_e32 v25, v9, v17
	v_mul_f32_e32 v22, v8, v18
	v_mul_f32_e32 v26, v9, v18
	v_mul_f32_e32 v23, v8, v19
	v_mul_f32_e32 v27, v9, v19
	v_exp_f32_e32 v20, v20
	v_exp_f32_e32 v21, v21
	v_exp_f32_e32 v22, v22
	v_exp_f32_e32 v23, v23
	v_exp_f32_e32 v24, v24
	v_exp_f32_e32 v25, v25
	v_exp_f32_e32 v26, v26
	v_exp_f32_e32 v27, v27
	v_cvt_pk_f16_f32 v32, v20, v21
	v_cvt_pk_f16_f32 v33, v22, v23
	v_cvt_pk_f16_f32 v64, v24, v25
	v_cvt_pk_f16_f32 v65, v26, v27
	v_add_f32_e32 v16, 0x40800000, v12
	v_add_f32_e32 v17, 0x40a00000, v12
	v_add_f32_e32 v18, 0x40c00000, v12
	v_add_f32_e32 v19, 0x40e00000, v12
	v_mul_f32_e32 v16, v16, v16
	v_mul_f32_e32 v17, v17, v17
	v_mul_f32_e32 v18, v18, v18
	v_mul_f32_e32 v19, v19, v19
	v_mul_f32_e32 v20, v8, v16
	v_mul_f32_e32 v24, v9, v16
	v_mul_f32_e32 v21, v8, v17
	v_mul_f32_e32 v25, v9, v17
	v_mul_f32_e32 v22, v8, v18
	v_mul_f32_e32 v26, v9, v18
	v_mul_f32_e32 v23, v8, v19
	v_mul_f32_e32 v27, v9, v19
	v_exp_f32_e32 v20, v20
	v_exp_f32_e32 v21, v21
	v_exp_f32_e32 v22, v22
	v_exp_f32_e32 v23, v23
	v_exp_f32_e32 v24, v24
	v_exp_f32_e32 v25, v25
	v_exp_f32_e32 v26, v26
	v_exp_f32_e32 v27, v27
	v_cvt_pk_f16_f32 v34, v20, v21
	v_cvt_pk_f16_f32 v35, v22, v23
	v_cvt_pk_f16_f32 v66, v24, v25
	v_cvt_pk_f16_f32 v67, v26, v27
	v_add_f32_e32 v16, 0x42000000, v12
	v_add_f32_e32 v17, 0x42040000, v12
	v_add_f32_e32 v18, 0x42080000, v12
	v_add_f32_e32 v19, 0x420c0000, v12
	v_mul_f32_e32 v16, v16, v16
	v_mul_f32_e32 v17, v17, v17
	v_mul_f32_e32 v18, v18, v18
	v_mul_f32_e32 v19, v19, v19
	v_mul_f32_e32 v20, v8, v16
	v_mul_f32_e32 v24, v9, v16
	v_mul_f32_e32 v21, v8, v17
	v_mul_f32_e32 v25, v9, v17
	v_mul_f32_e32 v22, v8, v18
	v_mul_f32_e32 v26, v9, v18
	v_mul_f32_e32 v23, v8, v19
	v_mul_f32_e32 v27, v9, v19
	v_exp_f32_e32 v20, v20
	v_exp_f32_e32 v21, v21
	v_exp_f32_e32 v22, v22
	v_exp_f32_e32 v23, v23
	v_exp_f32_e32 v24, v24
	v_exp_f32_e32 v25, v25
	v_exp_f32_e32 v26, v26
	v_exp_f32_e32 v27, v27
	v_cvt_pk_f16_f32 v36, v20, v21
	v_cvt_pk_f16_f32 v37, v22, v23
	v_cvt_pk_f16_f32 v68, v24, v25
	v_cvt_pk_f16_f32 v69, v26, v27
	v_add_f32_e32 v16, 0x42100000, v12
	v_add_f32_e32 v17, 0x42140000, v12
	v_add_f32_e32 v18, 0x42180000, v12
	v_add_f32_e32 v19, 0x421c0000, v12
	v_mul_f32_e32 v16, v16, v16
	v_mul_f32_e32 v17, v17, v17
	v_mul_f32_e32 v18, v18, v18
	v_mul_f32_e32 v19, v19, v19
	v_mul_f32_e32 v20, v8, v16
	v_mul_f32_e32 v24, v9, v16
	v_mul_f32_e32 v21, v8, v17
	v_mul_f32_e32 v25, v9, v17
	v_mul_f32_e32 v22, v8, v18
	v_mul_f32_e32 v26, v9, v18
	v_mul_f32_e32 v23, v8, v19
	v_mul_f32_e32 v27, v9, v19
	v_exp_f32_e32 v20, v20
	v_exp_f32_e32 v21, v21
	v_exp_f32_e32 v22, v22
	v_exp_f32_e32 v23, v23
	v_exp_f32_e32 v24, v24
	v_exp_f32_e32 v25, v25
	v_exp_f32_e32 v26, v26
	v_exp_f32_e32 v27, v27
	v_cvt_pk_f16_f32 v38, v20, v21
	v_cvt_pk_f16_f32 v39, v22, v23
	v_cvt_pk_f16_f32 v70, v24, v25
	v_cvt_pk_f16_f32 v71, v26, v27
	v_add_u32_e32 v6, 0x8000, v6
	global_load_dwordx4 v[160:163], v6, s[12:13] offset:0 nt
	global_load_dwordx4 v[164:167], v6, s[12:13] offset:1024 nt
	global_load_dwordx4 v[168:171], v6, s[12:13] offset:2048 nt
	global_load_dwordx4 v[172:175], v6, s[12:13] offset:3072 nt
	v_add_f32_e32 v16, 0x42800000, v12
	v_add_f32_e32 v17, 0x42820000, v12
	v_add_f32_e32 v18, 0x42840000, v12
	v_add_f32_e32 v19, 0x42860000, v12
	v_mul_f32_e32 v16, v16, v16
	v_mul_f32_e32 v17, v17, v17
	v_mul_f32_e32 v18, v18, v18
	v_mul_f32_e32 v19, v19, v19
	v_mul_f32_e32 v20, v8, v16
	v_mul_f32_e32 v24, v9, v16
	v_mul_f32_e32 v21, v8, v17
	v_mul_f32_e32 v25, v9, v17
	v_mul_f32_e32 v22, v8, v18
	v_mul_f32_e32 v26, v9, v18
	v_mul_f32_e32 v23, v8, v19
	v_mul_f32_e32 v27, v9, v19
	v_exp_f32_e32 v20, v20
	v_exp_f32_e32 v21, v21
	v_exp_f32_e32 v22, v22
	v_exp_f32_e32 v23, v23
	v_exp_f32_e32 v24, v24
	v_exp_f32_e32 v25, v25
	v_exp_f32_e32 v26, v26
	v_exp_f32_e32 v27, v27
	v_cvt_pk_f16_f32 v40, v20, v21
	v_cvt_pk_f16_f32 v41, v22, v23
	v_cvt_pk_f16_f32 v72, v24, v25
	v_cvt_pk_f16_f32 v73, v26, v27
	v_add_f32_e32 v16, 0x42880000, v12
	v_add_f32_e32 v17, 0x428a0000, v12
	v_add_f32_e32 v18, 0x428c0000, v12
	v_add_f32_e32 v19, 0x428e0000, v12
	v_mul_f32_e32 v16, v16, v16
	v_mul_f32_e32 v17, v17, v17
	v_mul_f32_e32 v18, v18, v18
	v_mul_f32_e32 v19, v19, v19
	v_mul_f32_e32 v20, v8, v16
	v_mul_f32_e32 v24, v9, v16
	v_mul_f32_e32 v21, v8, v17
	v_mul_f32_e32 v25, v9, v17
	v_mul_f32_e32 v22, v8, v18
	v_mul_f32_e32 v26, v9, v18
	v_mul_f32_e32 v23, v8, v19
	v_mul_f32_e32 v27, v9, v19
	v_exp_f32_e32 v20, v20
	v_exp_f32_e32 v21, v21
	v_exp_f32_e32 v22, v22
	v_exp_f32_e32 v23, v23
	v_exp_f32_e32 v24, v24
	v_exp_f32_e32 v25, v25
	v_exp_f32_e32 v26, v26
	v_exp_f32_e32 v27, v27
	v_cvt_pk_f16_f32 v42, v20, v21
	v_cvt_pk_f16_f32 v43, v22, v23
	v_cvt_pk_f16_f32 v74, v24, v25
	v_cvt_pk_f16_f32 v75, v26, v27
	v_add_f32_e32 v16, 0x42c00000, v12
	v_add_f32_e32 v17, 0x42c20000, v12
	v_add_f32_e32 v18, 0x42c40000, v12
	v_add_f32_e32 v19, 0x42c60000, v12
	v_mul_f32_e32 v16, v16, v16
	v_mul_f32_e32 v17, v17, v17
	v_mul_f32_e32 v18, v18, v18
	v_mul_f32_e32 v19, v19, v19
	v_mul_f32_e32 v20, v8, v16
	v_mul_f32_e32 v24, v9, v16
	v_mul_f32_e32 v21, v8, v17
	v_mul_f32_e32 v25, v9, v17
	v_mul_f32_e32 v22, v8, v18
	v_mul_f32_e32 v26, v9, v18
	v_mul_f32_e32 v23, v8, v19
	v_mul_f32_e32 v27, v9, v19
	v_exp_f32_e32 v20, v20
	v_exp_f32_e32 v21, v21
	v_exp_f32_e32 v22, v22
	v_exp_f32_e32 v23, v23
	v_exp_f32_e32 v24, v24
	v_exp_f32_e32 v25, v25
	v_exp_f32_e32 v26, v26
	v_exp_f32_e32 v27, v27
	v_cvt_pk_f16_f32 v44, v20, v21
	v_cvt_pk_f16_f32 v45, v22, v23
	v_cvt_pk_f16_f32 v76, v24, v25
	v_cvt_pk_f16_f32 v77, v26, v27
	v_add_f32_e32 v16, 0x42c80000, v12
	v_add_f32_e32 v17, 0x42ca0000, v12
	v_add_f32_e32 v18, 0x42cc0000, v12
	v_add_f32_e32 v19, 0x42ce0000, v12
	v_mul_f32_e32 v16, v16, v16
	v_mul_f32_e32 v17, v17, v17
	v_mul_f32_e32 v18, v18, v18
	v_mul_f32_e32 v19, v19, v19
	v_mul_f32_e32 v20, v8, v16
	v_mul_f32_e32 v24, v9, v16
	v_mul_f32_e32 v21, v8, v17
	v_mul_f32_e32 v25, v9, v17
	v_mul_f32_e32 v22, v8, v18
	v_mul_f32_e32 v26, v9, v18
	v_mul_f32_e32 v23, v8, v19
	v_mul_f32_e32 v27, v9, v19
	v_exp_f32_e32 v20, v20
	v_exp_f32_e32 v21, v21
	v_exp_f32_e32 v22, v22
	v_exp_f32_e32 v23, v23
	v_exp_f32_e32 v24, v24
	v_exp_f32_e32 v25, v25
	v_exp_f32_e32 v26, v26
	v_exp_f32_e32 v27, v27
	v_cvt_pk_f16_f32 v46, v20, v21
	v_cvt_pk_f16_f32 v47, v22, v23
	v_cvt_pk_f16_f32 v78, v24, v25
	v_cvt_pk_f16_f32 v79, v26, v27
	v_add_u32_e32 v6, 0x8000, v6
	global_load_dwordx4 v[176:179], v6, s[12:13] offset:0 nt
	global_load_dwordx4 v[180:183], v6, s[12:13] offset:1024 nt
	global_load_dwordx4 v[184:187], v6, s[12:13] offset:2048 nt
	global_load_dwordx4 v[188:191], v6, s[12:13] offset:3072 nt
	v_mul_f32_e32 v16, v2, v2
	v_add_f32_e32 v17, 0x3f800000, v2
	v_add_f32_e32 v18, 0x40000000, v2
	v_add_f32_e32 v19, 0x40400000, v2
	v_mul_f32_e32 v17, v17, v17
	v_mul_f32_e32 v18, v18, v18
	v_mul_f32_e32 v19, v19, v19
	v_mul_f32_e32 v20, v28, v16
	v_mul_f32_e32 v24, v29, v16
	v_mul_f32_e32 v21, v28, v17
	v_mul_f32_e32 v25, v29, v17
	v_mul_f32_e32 v22, v28, v18
	v_mul_f32_e32 v26, v29, v18
	v_mul_f32_e32 v23, v28, v19
	v_mul_f32_e32 v27, v29, v19
	v_exp_f32_e32 v20, v20
	v_exp_f32_e32 v21, v21
	v_exp_f32_e32 v22, v22
	v_exp_f32_e32 v23, v23
	v_exp_f32_e32 v24, v24
	v_exp_f32_e32 v25, v25
	v_exp_f32_e32 v26, v26
	v_exp_f32_e32 v27, v27
	v_cvt_pk_f16_f32 v48, v20, v21
	v_cvt_pk_f16_f32 v49, v22, v23
	v_cvt_pk_f16_f32 v80, v24, v25
	v_cvt_pk_f16_f32 v81, v26, v27
	v_add_f32_e32 v16, 0x40800000, v2
	v_add_f32_e32 v17, 0x40a00000, v2
	v_add_f32_e32 v18, 0x40c00000, v2
	v_add_f32_e32 v19, 0x40e00000, v2
	v_mul_f32_e32 v16, v16, v16
	v_mul_f32_e32 v17, v17, v17
	v_mul_f32_e32 v18, v18, v18
	v_mul_f32_e32 v19, v19, v19
	v_mul_f32_e32 v20, v28, v16
	v_mul_f32_e32 v24, v29, v16
	v_mul_f32_e32 v21, v28, v17
	v_mul_f32_e32 v25, v29, v17
	v_mul_f32_e32 v22, v28, v18
	v_mul_f32_e32 v26, v29, v18
	v_mul_f32_e32 v23, v28, v19
	v_mul_f32_e32 v27, v29, v19
	v_exp_f32_e32 v20, v20
	v_exp_f32_e32 v21, v21
	v_exp_f32_e32 v22, v22
	v_exp_f32_e32 v23, v23
	v_exp_f32_e32 v24, v24
	v_exp_f32_e32 v25, v25
	v_exp_f32_e32 v26, v26
	v_exp_f32_e32 v27, v27
	v_cvt_pk_f16_f32 v50, v20, v21
	v_cvt_pk_f16_f32 v51, v22, v23
	v_cvt_pk_f16_f32 v82, v24, v25
	v_cvt_pk_f16_f32 v83, v26, v27
	v_add_f32_e32 v16, 0x42000000, v2
	v_add_f32_e32 v17, 0x42040000, v2
	v_add_f32_e32 v18, 0x42080000, v2
	v_add_f32_e32 v19, 0x420c0000, v2
	v_mul_f32_e32 v16, v16, v16
	v_mul_f32_e32 v17, v17, v17
	v_mul_f32_e32 v18, v18, v18
	v_mul_f32_e32 v19, v19, v19
	v_mul_f32_e32 v20, v28, v16
	v_mul_f32_e32 v24, v29, v16
	v_mul_f32_e32 v21, v28, v17
	v_mul_f32_e32 v25, v29, v17
	v_mul_f32_e32 v22, v28, v18
	v_mul_f32_e32 v26, v29, v18
	v_mul_f32_e32 v23, v28, v19
	v_mul_f32_e32 v27, v29, v19
	v_exp_f32_e32 v20, v20
	v_exp_f32_e32 v21, v21
	v_exp_f32_e32 v22, v22
	v_exp_f32_e32 v23, v23
	v_exp_f32_e32 v24, v24
	v_exp_f32_e32 v25, v25
	v_exp_f32_e32 v26, v26
	v_exp_f32_e32 v27, v27
	v_cvt_pk_f16_f32 v52, v20, v21
	v_cvt_pk_f16_f32 v53, v22, v23
	v_cvt_pk_f16_f32 v84, v24, v25
	v_cvt_pk_f16_f32 v85, v26, v27
	v_add_f32_e32 v16, 0x42100000, v2
	v_add_f32_e32 v17, 0x42140000, v2
	v_add_f32_e32 v18, 0x42180000, v2
	v_add_f32_e32 v19, 0x421c0000, v2
	v_mul_f32_e32 v16, v16, v16
	v_mul_f32_e32 v17, v17, v17
	v_mul_f32_e32 v18, v18, v18
	v_mul_f32_e32 v19, v19, v19
	v_mul_f32_e32 v20, v28, v16
	v_mul_f32_e32 v24, v29, v16
	v_mul_f32_e32 v21, v28, v17
	v_mul_f32_e32 v25, v29, v17
	v_mul_f32_e32 v22, v28, v18
	v_mul_f32_e32 v26, v29, v18
	v_mul_f32_e32 v23, v28, v19
	v_mul_f32_e32 v27, v29, v19
	v_exp_f32_e32 v20, v20
	v_exp_f32_e32 v21, v21
	v_exp_f32_e32 v22, v22
	v_exp_f32_e32 v23, v23
	v_exp_f32_e32 v24, v24
	v_exp_f32_e32 v25, v25
	v_exp_f32_e32 v26, v26
	v_exp_f32_e32 v27, v27
	v_cvt_pk_f16_f32 v54, v20, v21
	v_cvt_pk_f16_f32 v55, v22, v23
	v_cvt_pk_f16_f32 v86, v24, v25
	v_cvt_pk_f16_f32 v87, v26, v27
	v_add_u32_e32 v6, 0x8000, v6
	global_load_dwordx4 v[192:195], v6, s[12:13] offset:0 nt
	global_load_dwordx4 v[196:199], v6, s[12:13] offset:1024 nt
	global_load_dwordx4 v[200:203], v6, s[12:13] offset:2048 nt
	global_load_dwordx4 v[204:207], v6, s[12:13] offset:3072 nt
	v_add_f32_e32 v16, 0x42800000, v2
	v_add_f32_e32 v17, 0x42820000, v2
	v_add_f32_e32 v18, 0x42840000, v2
	v_add_f32_e32 v19, 0x42860000, v2
	v_mul_f32_e32 v16, v16, v16
	v_mul_f32_e32 v17, v17, v17
	v_mul_f32_e32 v18, v18, v18
	v_mul_f32_e32 v19, v19, v19
	v_mul_f32_e32 v20, v28, v16
	v_mul_f32_e32 v24, v29, v16
	v_mul_f32_e32 v21, v28, v17
	v_mul_f32_e32 v25, v29, v17
	v_mul_f32_e32 v22, v28, v18
	v_mul_f32_e32 v26, v29, v18
	v_mul_f32_e32 v23, v28, v19
	v_mul_f32_e32 v27, v29, v19
	v_exp_f32_e32 v20, v20
	v_exp_f32_e32 v21, v21
	v_exp_f32_e32 v22, v22
	v_exp_f32_e32 v23, v23
	v_exp_f32_e32 v24, v24
	v_exp_f32_e32 v25, v25
	v_exp_f32_e32 v26, v26
	v_exp_f32_e32 v27, v27
	v_cvt_pk_f16_f32 v56, v20, v21
	v_cvt_pk_f16_f32 v57, v22, v23
	v_cvt_pk_f16_f32 v88, v24, v25
	v_cvt_pk_f16_f32 v89, v26, v27
	v_add_f32_e32 v16, 0x42880000, v2
	v_add_f32_e32 v17, 0x428a0000, v2
	v_add_f32_e32 v18, 0x428c0000, v2
	v_add_f32_e32 v19, 0x428e0000, v2
	v_mul_f32_e32 v16, v16, v16
	v_mul_f32_e32 v17, v17, v17
	v_mul_f32_e32 v18, v18, v18
	v_mul_f32_e32 v19, v19, v19
	v_mul_f32_e32 v20, v28, v16
	v_mul_f32_e32 v24, v29, v16
	v_mul_f32_e32 v21, v28, v17
	v_mul_f32_e32 v25, v29, v17
	v_mul_f32_e32 v22, v28, v18
	v_mul_f32_e32 v26, v29, v18
	v_mul_f32_e32 v23, v28, v19
	v_mul_f32_e32 v27, v29, v19
	v_exp_f32_e32 v20, v20
	v_exp_f32_e32 v21, v21
	v_exp_f32_e32 v22, v22
	v_exp_f32_e32 v23, v23
	v_exp_f32_e32 v24, v24
	v_exp_f32_e32 v25, v25
	v_exp_f32_e32 v26, v26
	v_exp_f32_e32 v27, v27
	v_cvt_pk_f16_f32 v58, v20, v21
	v_cvt_pk_f16_f32 v59, v22, v23
	v_cvt_pk_f16_f32 v90, v24, v25
	v_cvt_pk_f16_f32 v91, v26, v27
	v_add_f32_e32 v16, 0x42c00000, v2
	v_add_f32_e32 v17, 0x42c20000, v2
	v_add_f32_e32 v18, 0x42c40000, v2
	v_add_f32_e32 v19, 0x42c60000, v2
	v_mul_f32_e32 v16, v16, v16
	v_mul_f32_e32 v17, v17, v17
	v_mul_f32_e32 v18, v18, v18
	v_mul_f32_e32 v19, v19, v19
	v_mul_f32_e32 v20, v28, v16
	v_mul_f32_e32 v24, v29, v16
	v_mul_f32_e32 v21, v28, v17
	v_mul_f32_e32 v25, v29, v17
	v_mul_f32_e32 v22, v28, v18
	v_mul_f32_e32 v26, v29, v18
	v_mul_f32_e32 v23, v28, v19
	v_mul_f32_e32 v27, v29, v19
	v_exp_f32_e32 v20, v20
	v_exp_f32_e32 v21, v21
	v_exp_f32_e32 v22, v22
	v_exp_f32_e32 v23, v23
	v_exp_f32_e32 v24, v24
	v_exp_f32_e32 v25, v25
	v_exp_f32_e32 v26, v26
	v_exp_f32_e32 v27, v27
	v_cvt_pk_f16_f32 v60, v20, v21
	v_cvt_pk_f16_f32 v61, v22, v23
	v_cvt_pk_f16_f32 v92, v24, v25
	v_cvt_pk_f16_f32 v93, v26, v27
	v_add_f32_e32 v16, 0x42c80000, v2
	v_add_f32_e32 v17, 0x42ca0000, v2
	v_add_f32_e32 v18, 0x42cc0000, v2
	v_add_f32_e32 v19, 0x42ce0000, v2
	v_mul_f32_e32 v16, v16, v16
	v_mul_f32_e32 v17, v17, v17
	v_mul_f32_e32 v18, v18, v18
	v_mul_f32_e32 v19, v19, v19
	v_mul_f32_e32 v20, v28, v16
	v_mul_f32_e32 v24, v29, v16
	v_mul_f32_e32 v21, v28, v17
	v_mul_f32_e32 v25, v29, v17
	v_mul_f32_e32 v22, v28, v18
	v_mul_f32_e32 v26, v29, v18
	v_mul_f32_e32 v23, v28, v19
	v_mul_f32_e32 v27, v29, v19
	v_exp_f32_e32 v20, v20
	v_exp_f32_e32 v21, v21
	v_exp_f32_e32 v22, v22
	v_exp_f32_e32 v23, v23
	v_exp_f32_e32 v24, v24
	v_exp_f32_e32 v25, v25
	v_exp_f32_e32 v26, v26
	v_exp_f32_e32 v27, v27
	v_cvt_pk_f16_f32 v62, v20, v21
	v_cvt_pk_f16_f32 v63, v22, v23
	v_cvt_pk_f16_f32 v94, v24, v25
	v_cvt_pk_f16_f32 v95, v26, v27
	v_add_u32_e32 v6, 0x8000, v6
	global_load_dwordx4 v[208:211], v6, s[12:13] offset:0 nt
	global_load_dwordx4 v[212:215], v6, s[12:13] offset:1024 nt
	global_load_dwordx4 v[216:219], v6, s[12:13] offset:2048 nt
	global_load_dwordx4 v[220:223], v6, s[12:13] offset:3072 nt
	v_mul_f32_e32 v16, v13, v13
	v_add_f32_e32 v17, 0x3f800000, v13
	v_add_f32_e32 v18, 0x40000000, v13
	v_add_f32_e32 v19, 0x40400000, v13
	v_mul_f32_e32 v17, v17, v17
	v_mul_f32_e32 v18, v18, v18
	v_mul_f32_e32 v19, v19, v19
	v_mul_f32_e32 v20, v8, v16
	v_mul_f32_e32 v24, v9, v16
	v_mul_f32_e32 v21, v8, v17
	v_mul_f32_e32 v25, v9, v17
	v_mul_f32_e32 v22, v8, v18
	v_mul_f32_e32 v26, v9, v18
	v_mul_f32_e32 v23, v8, v19
	v_mul_f32_e32 v27, v9, v19
	v_exp_f32_e32 v20, v20
	v_exp_f32_e32 v21, v21
	v_exp_f32_e32 v22, v22
	v_exp_f32_e32 v23, v23
	v_exp_f32_e32 v24, v24
	v_exp_f32_e32 v25, v25
	v_exp_f32_e32 v26, v26
	v_exp_f32_e32 v27, v27
	v_mul_f32_e32 v96, v10, v20
	v_mul_f32_e32 v97, v10, v21
	v_mul_f32_e32 v98, v10, v22
	v_mul_f32_e32 v99, v10, v23
	v_mul_f32_e32 v112, v11, v24
	v_mul_f32_e32 v113, v11, v25
	v_mul_f32_e32 v114, v11, v26
	v_mul_f32_e32 v115, v11, v27
	v_add_f32_e32 v16, 0x41800000, v13
	v_add_f32_e32 v17, 0x41880000, v13
	v_add_f32_e32 v18, 0x41900000, v13
	v_add_f32_e32 v19, 0x41980000, v13
	v_mul_f32_e32 v16, v16, v16
	v_mul_f32_e32 v17, v17, v17
	v_mul_f32_e32 v18, v18, v18
	v_mul_f32_e32 v19, v19, v19
	v_mul_f32_e32 v20, v8, v16
	v_mul_f32_e32 v24, v9, v16
	v_mul_f32_e32 v21, v8, v17
	v_mul_f32_e32 v25, v9, v17
	v_mul_f32_e32 v22, v8, v18
	v_mul_f32_e32 v26, v9, v18
	v_mul_f32_e32 v23, v8, v19
	v_mul_f32_e32 v27, v9, v19
	v_exp_f32_e32 v20, v20
	v_exp_f32_e32 v21, v21
	v_exp_f32_e32 v22, v22
	v_exp_f32_e32 v23, v23
	v_exp_f32_e32 v24, v24
	v_exp_f32_e32 v25, v25
	v_exp_f32_e32 v26, v26
	v_exp_f32_e32 v27, v27
	v_mul_f32_e32 v100, v10, v20
	v_mul_f32_e32 v101, v10, v21
	v_mul_f32_e32 v102, v10, v22
	v_mul_f32_e32 v103, v10, v23
	v_mul_f32_e32 v116, v11, v24
	v_mul_f32_e32 v117, v11, v25
	v_mul_f32_e32 v118, v11, v26
	v_mul_f32_e32 v119, v11, v27
	v_add_u32_e32 v6, 0x8000, v6
	global_load_dwordx4 v[224:227], v6, s[12:13] offset:0 nt
	global_load_dwordx4 v[228:231], v6, s[12:13] offset:1024 nt
	global_load_dwordx4 v[232:235], v6, s[12:13] offset:2048 nt
	global_load_dwordx4 v[236:239], v6, s[12:13] offset:3072 nt
	v_mul_f32_e32 v16, v3, v3
	v_add_f32_e32 v17, 0x3f800000, v3
	v_add_f32_e32 v18, 0x40000000, v3
	v_add_f32_e32 v19, 0x40400000, v3
	v_mul_f32_e32 v17, v17, v17
	v_mul_f32_e32 v18, v18, v18
	v_mul_f32_e32 v19, v19, v19
	v_mul_f32_e32 v20, v28, v16
	v_mul_f32_e32 v24, v29, v16
	v_mul_f32_e32 v21, v28, v17
	v_mul_f32_e32 v25, v29, v17
	v_mul_f32_e32 v22, v28, v18
	v_mul_f32_e32 v26, v29, v18
	v_mul_f32_e32 v23, v28, v19
	v_mul_f32_e32 v27, v29, v19
	v_exp_f32_e32 v20, v20
	v_exp_f32_e32 v21, v21
	v_exp_f32_e32 v22, v22
	v_exp_f32_e32 v23, v23
	v_exp_f32_e32 v24, v24
	v_exp_f32_e32 v25, v25
	v_exp_f32_e32 v26, v26
	v_exp_f32_e32 v27, v27
	v_mul_f32_e32 v104, v30, v20
	v_mul_f32_e32 v105, v30, v21
	v_mul_f32_e32 v106, v30, v22
	v_mul_f32_e32 v107, v30, v23
	v_mul_f32_e32 v120, v31, v24
	v_mul_f32_e32 v121, v31, v25
	v_mul_f32_e32 v122, v31, v26
	v_mul_f32_e32 v123, v31, v27
	v_add_f32_e32 v16, 0x41800000, v3
	v_add_f32_e32 v17, 0x41880000, v3
	v_add_f32_e32 v18, 0x41900000, v3
	v_add_f32_e32 v19, 0x41980000, v3
	v_mul_f32_e32 v16, v16, v16
	v_mul_f32_e32 v17, v17, v17
	v_mul_f32_e32 v18, v18, v18
	v_mul_f32_e32 v19, v19, v19
	v_mul_f32_e32 v20, v28, v16
	v_mul_f32_e32 v24, v29, v16
	v_mul_f32_e32 v21, v28, v17
	v_mul_f32_e32 v25, v29, v17
	v_mul_f32_e32 v22, v28, v18
	v_mul_f32_e32 v26, v29, v18
	v_mul_f32_e32 v23, v28, v19
	v_mul_f32_e32 v27, v29, v19
	v_exp_f32_e32 v20, v20
	v_exp_f32_e32 v21, v21
	v_exp_f32_e32 v22, v22
	v_exp_f32_e32 v23, v23
	v_exp_f32_e32 v24, v24
	v_exp_f32_e32 v25, v25
	v_exp_f32_e32 v26, v26
	v_exp_f32_e32 v27, v27
	v_mul_f32_e32 v108, v30, v20
	v_mul_f32_e32 v109, v30, v21
	v_mul_f32_e32 v110, v30, v22
	v_mul_f32_e32 v111, v30, v23
	v_mul_f32_e32 v124, v31, v24
	v_mul_f32_e32 v125, v31, v25
	v_mul_f32_e32 v126, v31, v26
	v_mul_f32_e32 v127, v31, v27
	v_add_u32_e32 v6, 0x8000, v6
	global_load_dwordx4 v[240:243], v6, s[12:13] offset:0 nt
	global_load_dwordx4 v[244:247], v6, s[12:13] offset:1024 nt
	global_load_dwordx4 v[248:251], v6, s[12:13] offset:2048 nt
	global_load_dwordx4 v[252:255], v6, s[12:13] offset:3072 nt
	s_waitcnt vmcnt(28)
	v_add_f32_e32 v128, v128, v129
	v_add_f32_e32 v130, v130, v131
	v_add_f32_e32 v132, v132, v133
	v_add_f32_e32 v134, v134, v135
	v_add_f32_e32 v136, v136, v137
	v_add_f32_e32 v138, v138, v139
	v_add_f32_e32 v140, v140, v141
	v_add_f32_e32 v142, v142, v143
	v_add_f32_e32 v128, v128, v130
	v_add_f32_e32 v132, v132, v134
	v_add_f32_e32 v136, v136, v138
	v_add_f32_e32 v140, v140, v142
	v_cndmask_b32_e64 v130, v128, v132, s[30:31]
	v_cndmask_b32_e64 v134, v136, v140, s[30:31]
	v_cndmask_b32_e64 v129, v132, v128, s[30:31]
	v_cndmask_b32_e64 v133, v140, v136, s[30:31]
	v_add_f32_dpp v129, v130, v129 quad_perm:[1,0,3,2] row_mask:0xf bank_mask:0xf bound_ctrl:1
	v_add_f32_dpp v133, v134, v133 quad_perm:[1,0,3,2] row_mask:0xf bank_mask:0xf bound_ctrl:1
	v_cndmask_b32_e64 v135, v129, v133, s[32:33]
	v_cndmask_b32_e64 v131, v133, v129, s[32:33]
	s_nop 1
	v_add_f32_dpp v131, v135, v131 quad_perm:[2,3,0,1] row_mask:0xf bank_mask:0xf bound_ctrl:1
	v_cvt_f16_f32_e32 v131, v131
	ds_write_b16 v14, v131 offset:0
	s_waitcnt vmcnt(24)
	v_add_f32_e32 v144, v144, v145
	v_add_f32_e32 v146, v146, v147
	v_add_f32_e32 v148, v148, v149
	v_add_f32_e32 v150, v150, v151
	v_add_f32_e32 v152, v152, v153
	v_add_f32_e32 v154, v154, v155
	v_add_f32_e32 v156, v156, v157
	v_add_f32_e32 v158, v158, v159
	v_add_f32_e32 v144, v144, v146
	v_add_f32_e32 v148, v148, v150
	v_add_f32_e32 v152, v152, v154
	v_add_f32_e32 v156, v156, v158
	v_cndmask_b32_e64 v146, v144, v148, s[30:31]
	v_cndmask_b32_e64 v150, v152, v156, s[30:31]
	v_cndmask_b32_e64 v145, v148, v144, s[30:31]
	v_cndmask_b32_e64 v149, v156, v152, s[30:31]
	v_add_f32_dpp v145, v146, v145 quad_perm:[1,0,3,2] row_mask:0xf bank_mask:0xf bound_ctrl:1
	v_add_f32_dpp v149, v150, v149 quad_perm:[1,0,3,2] row_mask:0xf bank_mask:0xf bound_ctrl:1
	v_cndmask_b32_e64 v151, v145, v149, s[32:33]
	v_cndmask_b32_e64 v147, v149, v145, s[32:33]
	s_nop 1
	v_add_f32_dpp v147, v151, v147 quad_perm:[2,3,0,1] row_mask:0xf bank_mask:0xf bound_ctrl:1
	v_cvt_f16_f32_e32 v147, v147
	ds_write_b16 v14, v147 offset:1088
	s_waitcnt vmcnt(20)
	v_add_f32_e32 v160, v160, v161
	v_add_f32_e32 v162, v162, v163
	v_add_f32_e32 v164, v164, v165
	v_add_f32_e32 v166, v166, v167
	v_add_f32_e32 v168, v168, v169
	v_add_f32_e32 v170, v170, v171
	v_add_f32_e32 v172, v172, v173
	v_add_f32_e32 v174, v174, v175
	v_add_f32_e32 v160, v160, v162
	v_add_f32_e32 v164, v164, v166
	v_add_f32_e32 v168, v168, v170
	v_add_f32_e32 v172, v172, v174
	v_cndmask_b32_e64 v162, v160, v164, s[30:31]
	v_cndmask_b32_e64 v166, v168, v172, s[30:31]
	v_cndmask_b32_e64 v161, v164, v160, s[30:31]
	v_cndmask_b32_e64 v165, v172, v168, s[30:31]
	v_add_f32_dpp v161, v162, v161 quad_perm:[1,0,3,2] row_mask:0xf bank_mask:0xf bound_ctrl:1
	v_add_f32_dpp v165, v166, v165 quad_perm:[1,0,3,2] row_mask:0xf bank_mask:0xf bound_ctrl:1
	v_cndmask_b32_e64 v167, v161, v165, s[32:33]
	v_cndmask_b32_e64 v163, v165, v161, s[32:33]
	s_nop 1
	v_add_f32_dpp v163, v167, v163 quad_perm:[2,3,0,1] row_mask:0xf bank_mask:0xf bound_ctrl:1
	v_cvt_f16_f32_e32 v163, v163
	ds_write_b16 v14, v163 offset:2176
	s_waitcnt vmcnt(16)
	v_add_f32_e32 v176, v176, v177
	v_add_f32_e32 v178, v178, v179
	v_add_f32_e32 v180, v180, v181
	v_add_f32_e32 v182, v182, v183
	v_add_f32_e32 v184, v184, v185
	v_add_f32_e32 v186, v186, v187
	v_add_f32_e32 v188, v188, v189
	v_add_f32_e32 v190, v190, v191
	v_add_f32_e32 v176, v176, v178
	v_add_f32_e32 v180, v180, v182
	v_add_f32_e32 v184, v184, v186
	v_add_f32_e32 v188, v188, v190
	v_cndmask_b32_e64 v178, v176, v180, s[30:31]
	v_cndmask_b32_e64 v182, v184, v188, s[30:31]
	v_cndmask_b32_e64 v177, v180, v176, s[30:31]
	v_cndmask_b32_e64 v181, v188, v184, s[30:31]
	v_add_f32_dpp v177, v178, v177 quad_perm:[1,0,3,2] row_mask:0xf bank_mask:0xf bound_ctrl:1
	v_add_f32_dpp v181, v182, v181 quad_perm:[1,0,3,2] row_mask:0xf bank_mask:0xf bound_ctrl:1
	v_cndmask_b32_e64 v183, v177, v181, s[32:33]
	v_cndmask_b32_e64 v179, v181, v177, s[32:33]
	s_nop 1
	v_add_f32_dpp v179, v183, v179 quad_perm:[2,3,0,1] row_mask:0xf bank_mask:0xf bound_ctrl:1
	v_cvt_f16_f32_e32 v179, v179
	ds_write_b16 v14, v179 offset:3264
	s_mov_b32 s29, 0
	v_mov_b32_e32 v160, 0
	v_mov_b32_e32 v161, 0
	v_mov_b32_e32 v162, 0
	v_mov_b32_e32 v163, 0
	s_lshl_b32 s6, s6, 6
	s_add_i32 s6, s6, s7
	s_lshl_b32 s6, s6, 10
	v_add_u32_e32 v5, s6, v5
	s_branch .Lpass
.Lsecond_half:
	s_waitcnt vmcnt(12)
	v_add_f32_e32 v192, v192, v193
	v_add_f32_e32 v194, v194, v195
	v_add_f32_e32 v196, v196, v197
	v_add_f32_e32 v198, v198, v199
	v_add_f32_e32 v200, v200, v201
	v_add_f32_e32 v202, v202, v203
	v_add_f32_e32 v204, v204, v205
	v_add_f32_e32 v206, v206, v207
	v_add_f32_e32 v192, v192, v194
	v_add_f32_e32 v196, v196, v198
	v_add_f32_e32 v200, v200, v202
	v_add_f32_e32 v204, v204, v206
	v_cndmask_b32_e64 v194, v192, v196, s[30:31]
	v_cndmask_b32_e64 v198, v200, v204, s[30:31]
	v_cndmask_b32_e64 v193, v196, v192, s[30:31]
	v_cndmask_b32_e64 v197, v204, v200, s[30:31]
	v_add_f32_dpp v193, v194, v193 quad_perm:[1,0,3,2] row_mask:0xf bank_mask:0xf bound_ctrl:1
	v_add_f32_dpp v197, v198, v197 quad_perm:[1,0,3,2] row_mask:0xf bank_mask:0xf bound_ctrl:1
	v_cndmask_b32_e64 v199, v193, v197, s[32:33]
	v_cndmask_b32_e64 v195, v197, v193, s[32:33]
	s_nop 1
	v_add_f32_dpp v195, v199, v195 quad_perm:[2,3,0,1] row_mask:0xf bank_mask:0xf bound_ctrl:1
	v_cvt_f16_f32_e32 v195, v195
	ds_write_b16 v14, v195 offset:4352
	s_waitcnt vmcnt(8)
	v_add_f32_e32 v208, v208, v209
	v_add_f32_e32 v210, v210, v211
	v_add_f32_e32 v212, v212, v213
	v_add_f32_e32 v214, v214, v215
	v_add_f32_e32 v216, v216, v217
	v_add_f32_e32 v218, v218, v219
	v_add_f32_e32 v220, v220, v221
	v_add_f32_e32 v222, v222, v223
	v_add_f32_e32 v208, v208, v210
	v_add_f32_e32 v212, v212, v214
	v_add_f32_e32 v216, v216, v218
	v_add_f32_e32 v220, v220, v222
	v_cndmask_b32_e64 v210, v208, v212, s[30:31]
	v_cndmask_b32_e64 v214, v216, v220, s[30:31]
	v_cndmask_b32_e64 v209, v212, v208, s[30:31]
	v_cndmask_b32_e64 v213, v220, v216, s[30:31]
	v_add_f32_dpp v209, v210, v209 quad_perm:[1,0,3,2] row_mask:0xf bank_mask:0xf bound_ctrl:1
	v_add_f32_dpp v213, v214, v213 quad_perm:[1,0,3,2] row_mask:0xf bank_mask:0xf bound_ctrl:1
	v_cndmask_b32_e64 v215, v209, v213, s[32:33]
	v_cndmask_b32_e64 v211, v213, v209, s[32:33]
	s_nop 1
	v_add_f32_dpp v211, v215, v211 quad_perm:[2,3,0,1] row_mask:0xf bank_mask:0xf bound_ctrl:1
	v_cvt_f16_f32_e32 v211, v211
	ds_write_b16 v14, v211 offset:5440
	s_waitcnt vmcnt(4)
	v_add_f32_e32 v224, v224, v225
	v_add_f32_e32 v226, v226, v227
	v_add_f32_e32 v228, v228, v229
	v_add_f32_e32 v230, v230, v231
	v_add_f32_e32 v232, v232, v233
	v_add_f32_e32 v234, v234, v235
	v_add_f32_e32 v236, v236, v237
	v_add_f32_e32 v238, v238, v239
	v_add_f32_e32 v224, v224, v226
	v_add_f32_e32 v228, v228, v230
	v_add_f32_e32 v232, v232, v234
	v_add_f32_e32 v236, v236, v238
	v_cndmask_b32_e64 v226, v224, v228, s[30:31]
	v_cndmask_b32_e64 v230, v232, v236, s[30:31]
	v_cndmask_b32_e64 v225, v228, v224, s[30:31]
	v_cndmask_b32_e64 v229, v236, v232, s[30:31]
	v_add_f32_dpp v225, v226, v225 quad_perm:[1,0,3,2] row_mask:0xf bank_mask:0xf bound_ctrl:1
	v_add_f32_dpp v229, v230, v229 quad_perm:[1,0,3,2] row_mask:0xf bank_mask:0xf bound_ctrl:1
	v_cndmask_b32_e64 v231, v225, v229, s[32:33]
	v_cndmask_b32_e64 v227, v229, v225, s[32:33]
	s_nop 1
	v_add_f32_dpp v227, v231, v227 quad_perm:[2,3,0,1] row_mask:0xf bank_mask:0xf bound_ctrl:1
	v_cvt_f16_f32_e32 v227, v227
	ds_write_b16 v14, v227 offset:6528
	s_waitcnt vmcnt(0)
	v_add_f32_e32 v240, v240, v241
	v_add_f32_e32 v242, v242, v243
	v_add_f32_e32 v244, v244, v245
	v_add_f32_e32 v246, v246, v247
	v_add_f32_e32 v248, v248, v249
	v_add_f32_e32 v250, v250, v251
	v_add_f32_e32 v252, v252, v253
	v_add_f32_e32 v254, v254, v255
	v_add_f32_e32 v240, v240, v242
	v_add_f32_e32 v244, v244, v246
	v_add_f32_e32 v248, v248, v250
	v_add_f32_e32 v252, v252, v254
	v_cndmask_b32_e64 v242, v240, v244, s[30:31]
	v_cndmask_b32_e64 v246, v248, v252, s[30:31]
	v_cndmask_b32_e64 v241, v244, v240, s[30:31]
	v_cndmask_b32_e64 v245, v252, v248, s[30:31]
	v_add_f32_dpp v241, v242, v241 quad_perm:[1,0,3,2] row_mask:0xf bank_mask:0xf bound_ctrl:1
	v_add_f32_dpp v245, v246, v245 quad_perm:[1,0,3,2] row_mask:0xf bank_mask:0xf bound_ctrl:1
	v_cndmask_b32_e64 v247, v241, v245, s[32:33]
	v_cndmask_b32_e64 v243, v245, v241, s[32:33]
	s_nop 1
	v_add_f32_dpp v243, v247, v243 quad_perm:[2,3,0,1] row_mask:0xf bank_mask:0xf bound_ctrl:1
	v_cvt_f16_f32_e32 v243, v243
	ds_write_b16 v14, v243 offset:7616
.Lpass:
	s_waitcnt lgkmcnt(0)
	s_barrier
	ds_read_b128 v[144:147], v15 offset:0
	ds_read_b128 v[148:151], v15 offset:64
	ds_read_b128 v[152:155], v15 offset:128
	ds_read_b128 v[156:159], v15 offset:192
	s_waitcnt lgkmcnt(3)
	v_mfma_f32_16x16x32_f16 v[128:131], v[144:147], v[32:35], 0
	v_mfma_f32_16x16x32_f16 v[136:139], v[144:147], v[64:67], 0
	v_mfma_f32_16x16x32_f16 v[132:135], v[144:147], v[48:51], 0
	v_mfma_f32_16x16x32_f16 v[140:143], v[144:147], v[80:83], 0
	s_waitcnt lgkmcnt(2)
	v_mfma_f32_16x16x32_f16 v[128:131], v[148:151], v[36:39], v[128:131]
	v_mfma_f32_16x16x32_f16 v[136:139], v[148:151], v[68:71], v[136:139]
	v_mfma_f32_16x16x32_f16 v[132:135], v[148:151], v[52:55], v[132:135]
	v_mfma_f32_16x16x32_f16 v[140:143], v[148:151], v[84:87], v[140:143]
	s_waitcnt lgkmcnt(1)
	v_mfma_f32_16x16x32_f16 v[128:131], v[152:155], v[40:43], v[128:131]
	v_mfma_f32_16x16x32_f16 v[136:139], v[152:155], v[72:75], v[136:139]
	v_mfma_f32_16x16x32_f16 v[132:135], v[152:155], v[56:59], v[132:135]
	v_mfma_f32_16x16x32_f16 v[140:143], v[152:155], v[88:91], v[140:143]
	s_waitcnt lgkmcnt(0)
	v_mfma_f32_16x16x32_f16 v[128:131], v[156:159], v[44:47], v[128:131]
	v_mfma_f32_16x16x32_f16 v[136:139], v[156:159], v[76:79], v[136:139]
	v_mfma_f32_16x16x32_f16 v[132:135], v[156:159], v[60:63], v[132:135]
	v_mfma_f32_16x16x32_f16 v[140:143], v[156:159], v[92:95], v[140:143]
	s_nop 15
	v_fma_f32 v160, v96, v128, v160
	v_fma_f32 v161, -v112, v136, v161
	v_fma_f32 v162, v104, v132, v162
	v_fma_f32 v163, -v120, v140, v163
	v_fma_f32 v160, v97, v129, v160
	v_fma_f32 v161, -v113, v137, v161
	v_fma_f32 v162, v105, v133, v162
	v_fma_f32 v163, -v121, v141, v163
	v_fma_f32 v160, v98, v130, v160
	v_fma_f32 v161, -v114, v138, v161
	v_fma_f32 v162, v106, v134, v162
	v_fma_f32 v163, -v122, v142, v163
	v_fma_f32 v160, v99, v131, v160
	v_fma_f32 v161, -v115, v139, v161
	v_fma_f32 v162, v107, v135, v162
	v_fma_f32 v163, -v123, v143, v163
	v_add_f32_e32 v164, v160, v161
	v_add_f32_e32 v165, v162, v163
	v_cmp_gt_u32_e32 vcc, 32, v1
	s_cmp_eq_u32 s29, 1
	v_permlane16_swap_b32_e32 v164, v165
	s_nop 0
	v_add_f32_e32 v164, v164, v165
	v_mov_b32_e32 v165, v164
	s_nop 1
	v_permlane32_swap_b32_e32 v164, v165
	s_nop 0
	v_add_f32_e32 v164, v164, v165
	s_cbranch_scc1 .Lstore
	s_mov_b32 s29, 1
	v_add_u32_e32 v15, 0x1100, v15
	v_mov_b32_e32 v96, v100
	v_mov_b32_e32 v112, v116
	v_mov_b32_e32 v97, v101
	v_mov_b32_e32 v113, v117
	v_mov_b32_e32 v98, v102
	v_mov_b32_e32 v114, v118
	v_mov_b32_e32 v99, v103
	v_mov_b32_e32 v115, v119
	v_mov_b32_e32 v104, v108
	v_mov_b32_e32 v120, v124
	v_mov_b32_e32 v105, v109
	v_mov_b32_e32 v121, v125
	v_mov_b32_e32 v106, v110
	v_mov_b32_e32 v122, v126
	v_mov_b32_e32 v107, v111
	v_mov_b32_e32 v123, v127
	s_branch .Lsecond_half
.Lstore:
	s_and_saveexec_b64 s[2:3], vcc
	s_cbranch_execz .Ldog_main_done
	global_store_dword v5, v164, s[26:27]
